# TK threshold pass: all count reads issued together; N2 partial sum-of-squares reads batched (on top of v60)
# baseline (speedup 1.0000x reference)
; #define GAS __attribute__((address_space(1)))
; __device__ __forceinline__ unsigned pk2(float lo, float hi) { unsigned r; asm("v_cvt_pk_bf16_f32 %0, %1, %2" : "=v"(r) : "v"(lo), "v"(hi)); return r; }
; __device__ __forceinline__ void n2_phase(const Frame& F0, int L, int nrows) {
;     ...
;         __syncthreads();
;         float tot = 0.f;
; #pragma unroll
;         for (int w = 0; w < 8; ++w) tot += PSS[(par * 8 + w) * 16 + r];
;         const float rinv = __builtin_amdgcn_rsqf(tot * (1.0f / D) + EPS);
;         u32x4 ahi[4], alo[4];
; #pragma unroll
;         for (int s_ = 0; s_ < 4; ++s_) {
;             const f32x4 h0 = (v[s_][0] * rinv) * gs[s_][0] + sh[s_][0], h1 = (v[s_][1] * rinv) * gs[s_][1] + sh[s_][1];
;             u32x4 hi; hi.x = pk2(h0[0], h0[1]); hi.y = pk2(h0[2], h0[3]); hi.z = pk2(h1[0], h1[1]); hi.w = pk2(h1[2], h1[3]);
;             { u32x2 h8; h8.x = pg8::pack4_fp8(h0[0] * pg8::SC_H2, h0[1] * pg8::SC_H2, h0[2] * pg8::SC_H2, h0[3] * pg8::SC_H2); h8.y = pg8::pack4_fp8(h1[0] * pg8::SC_H2, h1[1] * pg8::SC_H2, h1[2] * pg8::SC_H2, h1[3] * pg8::SC_H2);
;               *(GAS u32x2*)(H8 + (size_t)row * D + c0 + 32 * s_) = h8; } ahi[s_] = hi;
;             alo[s_].x = pk2(h0[0] - bf_lo(hi.x), h0[1] - bf_hi(hi.x)); alo[s_].y = pk2(h0[2] - bf_lo(hi.y), h0[3] - bf_hi(hi.y));
;             alo[s_].z = pk2(h1[0] - bf_lo(hi.z), h1[1] - bf_hi(hi.z)); alo[s_].w = pk2(h1[2] - bf_lo(hi.w), h1[3] - bf_hi(hi.w)); }
.LBB0_1210:
	s_or_b64 exec, exec, s[0:1]
	v_add_u32_e32 v52, s7, v1
	s_waitcnt lgkmcnt(0)
	s_barrier
	ds_read2_b32 v[50:51], v52 offset1:16
	ds_read2_b32 v[54:55], v52 offset0:32 offset1:48
	ds_read2_b32 v[56:57], v52 offset0:64 offset1:80
	ds_read2_b32 v[58:59], v52 offset0:96 offset1:112
	v_ashrrev_i32_e32 v141, 31, v140
	s_lshl_b32 s3, s3, 13
	s_waitcnt lgkmcnt(0)
	v_add_f32_e32 v50, 0, v50
	v_add_f32_e32 v53, v50, v51
	v_add_f32_e32 v50, v53, v54
	v_add_f32_e32 v53, v50, v55
	v_add_f32_e32 v50, v53, v56
	v_add_f32_e32 v53, v50, v57
	v_add_f32_e32 v50, v53, v58
	v_add_f32_e32 v50, v50, v59
	v_fmamk_f32 v50, v50, 0x3a800000, v250
	v_rsq_f32_e32 v142, v50
	v_lshlrev_b64 v[50:51], 10, v[140:141]
	v_lshl_add_u64 v[140:141], v[86:87], 0, v[50:51]
	v_pk_mul_f32 v[50:51], v[142:143], v[154:155] op_sel_hi:[0,1]
	v_pk_fma_f32 v[56:57], v[108:109], v[50:51], v[22:23]
	v_pk_mul_f32 v[50:51], v[142:143], v[150:151] op_sel_hi:[0,1]
	v_mul_f32_e32 v58, 0x41000000, v56
	v_mul_f32_e32 v59, 0x41000000, v57
	v_med3_f32 v151, v58, s15, v212
	v_med3_f32 v59, v59, s15, v212
	v_mov_b32_e32 v58, 0
	v_pk_mul_f32 v[52:53], v[142:143], v[152:153] op_sel_hi:[0,1]
	v_cvt_pk_fp8_f32 v58, v151, v59
	v_pk_fma_f32 v[54:55], v[106:107], v[52:53], v[24:25]
	v_pk_fma_f32 v[60:61], v[112:113], v[50:51], v[18:19]
	v_mul_f32_e32 v139, 0x41000000, v54
	v_mul_f32_e32 v150, 0x41000000, v55
	v_med3_f32 v59, v139, s15, v212
	v_med3_f32 v139, v150, s15, v212
	v_cvt_pk_fp8_f32 v58, v59, v139 op_sel:[0,0,1]
	v_mul_f32_e32 v59, 0x41000000, v60
	v_mul_f32_e32 v139, 0x41000000, v61
	v_med3_f32 v152, v59, s15, v212
	v_med3_f32 v139, v139, s15, v212
	v_mov_b32_e32 v59, 0
	v_pk_mul_f32 v[52:53], v[142:143], v[148:149] op_sel_hi:[0,1]
	v_cvt_pk_fp8_f32 v59, v152, v139
	v_pk_fma_f32 v[148:149], v[110:111], v[52:53], v[20:21]
	v_cvt_pk_bf16_f32 v50, v56, v57
	v_cvt_pk_bf16_f32 v51, v54, v55
	v_cvt_pk_bf16_f32 v52, v60, v61
	v_pk_mul_f32 v[76:77], v[142:143], v[76:77] op_sel_hi:[0,1]
	v_mul_f32_e32 v150, 0x41000000, v148
	v_mul_f32_e32 v151, 0x41000000, v149
	v_med3_f32 v139, v150, s15, v212
	v_med3_f32 v150, v151, s15, v212
	v_cvt_pk_fp8_f32 v59, v139, v150 op_sel:[0,0,1]
	v_cvt_pk_bf16_f32 v53, v148, v149
	v_pk_mul_f32 v[74:75], v[142:143], v[74:75] op_sel_hi:[0,1]
	v_pk_mul_f32 v[68:69], v[142:143], v[68:69] op_sel_hi:[0,1]
	global_store_dwordx2 v[140:141], v[58:59], off
	v_lshlrev_b32_e32 v58, 16, v50
	v_sub_f32_e32 v56, v56, v58
	v_and_b32_e32 v58, 0xffff0000, v50
	v_sub_f32_e32 v57, v57, v58
	v_cvt_pk_bf16_f32 v58, v56, v57
	v_lshlrev_b32_e32 v56, 16, v51
	v_sub_f32_e32 v54, v54, v56
	v_and_b32_e32 v56, 0xffff0000, v51
	v_sub_f32_e32 v55, v55, v56
	v_cvt_pk_bf16_f32 v59, v54, v55
	v_lshlrev_b32_e32 v54, 16, v52
	v_and_b32_e32 v55, 0xffff0000, v52
	v_sub_f32_e32 v54, v60, v54
	v_sub_f32_e32 v55, v61, v55
	v_cvt_pk_bf16_f32 v60, v54, v55
	v_lshlrev_b32_e32 v54, 16, v53
	v_and_b32_e32 v55, 0xffff0000, v53
	v_sub_f32_e32 v54, v148, v54
	v_sub_f32_e32 v55, v149, v55
	v_cvt_pk_bf16_f32 v61, v54, v55
	v_pk_mul_f32 v[54:55], v[142:143], v[146:147] op_sel_hi:[0,1]
	v_pk_mul_f32 v[56:57], v[142:143], v[144:145] op_sel_hi:[0,1]
	v_pk_fma_f32 v[146:147], v[116:117], v[54:55], v[30:31]
	v_pk_fma_f32 v[144:145], v[114:115], v[56:57], v[32:33]
	v_pk_mul_f32 v[56:57], v[142:143], v[62:63] op_sel_hi:[0,1]
	v_mul_f32_e32 v62, 0x41000000, v146
	v_mul_f32_e32 v63, 0x41000000, v147
	v_med3_f32 v151, v62, s15, v212
	v_med3_f32 v63, v63, s15, v212
	v_mov_b32_e32 v62, 0
	v_cvt_pk_fp8_f32 v62, v151, v63
	v_pk_mul_f32 v[54:55], v[142:143], v[64:65] op_sel_hi:[0,1]
	v_mul_f32_e32 v139, 0x41000000, v144
	v_mul_f32_e32 v150, 0x41000000, v145
	v_pk_fma_f32 v[64:65], v[120:121], v[54:55], v[26:27]
	v_med3_f32 v63, v139, s15, v212
	v_med3_f32 v139, v150, s15, v212
	v_cvt_pk_fp8_f32 v62, v63, v139 op_sel:[0,0,1]
	v_mul_f32_e32 v63, 0x41000000, v64
	v_mul_f32_e32 v139, 0x41000000, v65
	v_med3_f32 v152, v63, s15, v212
	v_med3_f32 v139, v139, s15, v212
	v_mov_b32_e32 v63, 0
	v_cvt_pk_fp8_f32 v63, v152, v139
	v_pk_fma_f32 v[148:149], v[118:119], v[56:57], v[28:29]
	v_cvt_pk_bf16_f32 v54, v146, v147
	v_cvt_pk_bf16_f32 v55, v144, v145
	v_cvt_pk_bf16_f32 v56, v64, v65
	v_pk_mul_f32 v[66:67], v[142:143], v[66:67] op_sel_hi:[0,1]
	v_mul_f32_e32 v150, 0x41000000, v148
	v_mul_f32_e32 v151, 0x41000000, v149
	v_med3_f32 v139, v150, s15, v212
	v_med3_f32 v150, v151, s15, v212
	v_cvt_pk_fp8_f32 v63, v139, v150 op_sel:[0,0,1]
	v_and_b32_e32 v139, 0xffff0000, v55
	v_sub_f32_e32 v139, v145, v139
	v_cvt_pk_bf16_f32 v57, v148, v149
	global_store_dwordx2 v[140:141], v[62:63], off offset:32
	v_lshlrev_b32_e32 v62, 16, v54
	v_and_b32_e32 v63, 0xffff0000, v54
	v_sub_f32_e32 v62, v146, v62
	v_sub_f32_e32 v63, v147, v63
	v_cvt_pk_bf16_f32 v62, v62, v63
	v_lshlrev_b32_e32 v63, 16, v55
	v_sub_f32_e32 v63, v144, v63
	v_cvt_pk_bf16_f32 v63, v63, v139
	v_lshlrev_b32_e32 v139, 16, v56
	v_sub_f32_e32 v64, v64, v139
	v_and_b32_e32 v139, 0xffff0000, v56
	v_sub_f32_e32 v65, v65, v139
	v_cvt_pk_bf16_f32 v64, v64, v65
	v_lshlrev_b32_e32 v65, 16, v57
	v_and_b32_e32 v139, 0xffff0000, v57
	v_sub_f32_e32 v65, v148, v65
	v_sub_f32_e32 v139, v149, v139
	v_pk_fma_f32 v[144:145], v[122:123], v[74:75], v[40:41]
	v_pk_fma_f32 v[74:75], v[124:125], v[76:77], v[38:39]
	v_cvt_pk_bf16_f32 v65, v65, v139
	v_mul_f32_e32 v149, 0x41000000, v144
	v_mul_f32_e32 v139, 0x41000000, v74
	v_mul_f32_e32 v148, 0x41000000, v75
	v_med3_f32 v139, v139, s15, v212
	v_med3_f32 v151, v148, s15, v212
	v_mov_b32_e32 v148, 0
	v_cvt_pk_fp8_f32 v148, v139, v151
	v_mul_f32_e32 v150, 0x41000000, v145
	v_pk_fma_f32 v[76:77], v[128:129], v[68:69], v[34:35]
	v_med3_f32 v139, v149, s15, v212
; #define LAS __attribute__((address_space(3)))
; __device__ __forceinline__ void n2_phase(const Frame& F0, int L, int nrows) {
;     ...
;         f32x4 acc = (f32x4){0.f, 0.f, 0.f, 0.f};
; #pragma unroll
;         for (int s_ = 0; s_ < 4; ++s_) { const int o = ((16 * F.wave + 4 * s_ + kg) * 16 + r) * 8;
;             const bf16x8 bh = *(const LAS bf16x8*)(WH + o), bl = *(const LAS bf16x8*)(WL + o);
;             const bf16x8 ah = __builtin_bit_cast(bf16x8, ahi[s_]), al = __builtin_bit_cast(bf16x8, alo[s_]);
;             acc = __builtin_amdgcn_mfma_f32_16x16x32_bf16(ah, bh, acc, 0, 0, 0);
;             acc = __builtin_amdgcn_mfma_f32_16x16x32_bf16(ah, bl, acc, 0, 0, 0);
;             acc = __builtin_amdgcn_mfma_f32_16x16x32_bf16(al, bh, acc, 0, 0, 0); }
; #pragma unroll
;         for (int i = 0; i < 4; ++i) PLG[((par * 8 + F.wave) * 16 + 4 * kg + i) * 16 + r] = acc[i];
;         __syncthreads();
;         if (F.lane < 32) { const int rl = 2 * F.wave + (F.lane >> 4), e = F.lane & 15; float lg = 0.f;
; #pragma unroll
;             for (int w = 0; w < 8; ++w) lg += PLG[((par * 8 + w) * 16 + rl) * 16 + e];
;             float mx = lg;
; #pragma unroll
;             for (int o = 1; o < 16; o <<= 1) mx = fmaxf(mx, __shfl_xor(mx, o));
;             const float ex = __expf(lg - mx); float den = ex;
; #pragma unroll
;             for (int o = 1; o < 16; o <<= 1) den += __shfl_xor(den, o);
;             AFF[(size_t)(row0 + rl) * 16 + e] = ex / den; }
	v_med3_f32 v149, v150, s15, v212
	v_cvt_pk_fp8_f32 v148, v139, v149 op_sel:[0,0,1]
	v_mul_f32_e32 v139, 0x41000000, v76
	v_mul_f32_e32 v149, 0x41000000, v77
	v_med3_f32 v139, v139, s15, v212
	v_med3_f32 v152, v149, s15, v212
	v_mov_b32_e32 v149, 0
	v_cvt_pk_fp8_f32 v149, v139, v152
	v_pk_fma_f32 v[146:147], v[126:127], v[66:67], v[36:37]
	v_cvt_pk_bf16_f32 v66, v74, v75
	v_cvt_pk_bf16_f32 v67, v144, v145
	v_cvt_pk_bf16_f32 v68, v76, v77
	v_pk_mul_f32 v[80:81], v[142:143], v[80:81] op_sel_hi:[0,1]
	v_mul_f32_e32 v150, 0x41000000, v146
	v_mul_f32_e32 v151, 0x41000000, v147
	v_med3_f32 v139, v150, s15, v212
	v_med3_f32 v150, v151, s15, v212
	v_cvt_pk_fp8_f32 v149, v139, v150 op_sel:[0,0,1]
	v_lshlrev_b32_e32 v139, 16, v66
	v_sub_f32_e32 v74, v74, v139
	v_and_b32_e32 v139, 0xffff0000, v66
	v_sub_f32_e32 v75, v75, v139
	v_cvt_pk_bf16_f32 v74, v74, v75
	v_lshlrev_b32_e32 v75, 16, v67
	v_and_b32_e32 v139, 0xffff0000, v67
	v_sub_f32_e32 v75, v144, v75
	v_sub_f32_e32 v139, v145, v139
	v_cvt_pk_bf16_f32 v75, v75, v139
	v_lshlrev_b32_e32 v139, 16, v68
	v_sub_f32_e32 v76, v76, v139
	v_and_b32_e32 v139, 0xffff0000, v68
	v_sub_f32_e32 v77, v77, v139
	v_cvt_pk_bf16_f32 v69, v146, v147
	v_cvt_pk_bf16_f32 v76, v76, v77
	v_pk_mul_f32 v[78:79], v[142:143], v[78:79] op_sel_hi:[0,1]
	v_lshlrev_b32_e32 v77, 16, v69
	v_and_b32_e32 v139, 0xffff0000, v69
	v_sub_f32_e32 v77, v146, v77
	v_sub_f32_e32 v139, v147, v139
	v_pk_fma_f32 v[144:145], v[130:131], v[78:79], v[48:49]
	v_pk_fma_f32 v[78:79], v[132:133], v[80:81], v[46:47]
	v_cvt_pk_bf16_f32 v77, v77, v139
	v_pk_mul_f32 v[72:73], v[142:143], v[72:73] op_sel_hi:[0,1]
	v_pk_mul_f32 v[70:71], v[142:143], v[70:71] op_sel_hi:[0,1]
	v_mul_f32_e32 v139, 0x41000000, v78
	v_mul_f32_e32 v142, 0x41000000, v79
	global_store_dwordx2 v[140:141], v[148:149], off offset:64
	v_med3_f32 v139, v139, s15, v212
	v_med3_f32 v142, v142, s15, v212
	v_mov_b32_e32 v148, 0
	v_cvt_pk_fp8_f32 v148, v139, v142
	v_mul_f32_e32 v149, 0x41000000, v144
	v_mul_f32_e32 v150, 0x41000000, v145
	v_pk_fma_f32 v[80:81], v[136:137], v[72:73], v[42:43]
	v_med3_f32 v139, v149, s15, v212
	v_med3_f32 v142, v150, s15, v212
	v_cvt_pk_fp8_f32 v148, v139, v142 op_sel:[0,0,1]
	v_mul_f32_e32 v139, 0x41000000, v80
	v_mul_f32_e32 v142, 0x41000000, v81
	v_med3_f32 v139, v139, s15, v212
	v_med3_f32 v142, v142, s15, v212
	v_mov_b32_e32 v149, 0
	v_cvt_pk_fp8_f32 v149, v139, v142
	v_pk_fma_f32 v[146:147], v[134:135], v[70:71], v[44:45]
	v_cvt_pk_bf16_f32 v70, v78, v79
	v_cvt_pk_bf16_f32 v71, v144, v145
	v_cvt_pk_bf16_f32 v72, v80, v81
	s_nop 0
	v_mul_f32_e32 v150, 0x41000000, v146
	v_mul_f32_e32 v151, 0x41000000, v147
	v_med3_f32 v139, v150, s15, v212
	v_med3_f32 v142, v151, s15, v212
	v_cvt_pk_fp8_f32 v149, v139, v142 op_sel:[0,0,1]
	v_lshlrev_b32_e32 v139, 16, v70
	v_sub_f32_e32 v78, v78, v139
	v_and_b32_e32 v139, 0xffff0000, v70
	v_sub_f32_e32 v79, v79, v139
	v_cvt_pk_bf16_f32 v78, v78, v79
	v_lshlrev_b32_e32 v79, 16, v71
	v_and_b32_e32 v139, 0xffff0000, v71
	v_sub_f32_e32 v79, v144, v79
	v_sub_f32_e32 v139, v145, v139
	v_cvt_pk_bf16_f32 v79, v79, v139
	v_lshlrev_b32_e32 v139, 16, v72
	v_sub_f32_e32 v80, v80, v139
	v_and_b32_e32 v139, 0xffff0000, v72
	v_sub_f32_e32 v81, v81, v139
	v_cvt_pk_bf16_f32 v73, v146, v147
	global_store_dwordx2 v[140:141], v[148:149], off offset:96
	v_cvt_pk_bf16_f32 v80, v80, v81
	v_lshlrev_b32_e32 v81, 16, v73
	v_and_b32_e32 v139, 0xffff0000, v73
	v_sub_f32_e32 v81, v146, v81
	v_sub_f32_e32 v139, v147, v139
	v_mfma_f32_16x16x32_bf16 v[152:155], v[50:53], v[214:217], 0
	v_cvt_pk_bf16_f32 v81, v81, v139
	v_mfma_f32_16x16x32_bf16 v[50:53], v[50:53], v[218:221], v[152:155]
	v_mfma_f32_16x16x32_bf16 v[50:53], v[58:61], v[214:217], v[50:53]
	v_mfma_f32_16x16x32_bf16 v[50:53], v[54:57], v[222:225], v[50:53]
	v_mfma_f32_16x16x32_bf16 v[50:53], v[54:57], v[226:229], v[50:53]
	v_mfma_f32_16x16x32_bf16 v[50:53], v[62:65], v[222:225], v[50:53]
	v_mfma_f32_16x16x32_bf16 v[50:53], v[66:69], v[230:233], v[50:53]
	v_mfma_f32_16x16x32_bf16 v[50:53], v[66:69], v[234:237], v[50:53]
	v_mfma_f32_16x16x32_bf16 v[50:53], v[74:77], v[230:233], v[50:53]
	v_mfma_f32_16x16x32_bf16 v[50:53], v[70:73], v[238:241], v[50:53]
	v_mfma_f32_16x16x32_bf16 v[50:53], v[70:73], v[242:245], v[50:53]
	v_mfma_f32_16x16x32_bf16 v[50:53], v[78:81], v[238:241], v[50:53]
	v_add_u32_e32 v54, s3, v157
	s_nop 6
	ds_write2_b32 v54, v50, v51 offset1:16
	ds_write2_b32 v54, v52, v53 offset0:32 offset1:48
	s_waitcnt lgkmcnt(0)
	s_barrier
	s_and_saveexec_b64 s[0:1], s[38:39]
	s_cbranch_execz .LBB0_1212
	v_add_u32_e32 v52, s3, v156
	ds_read2st64_b32 v[50:51], v52 offset1:4
	ds_read2st64_b32 v[54:55], v52 offset0:8 offset1:12
	ds_read2st64_b32 v[56:57], v52 offset0:16 offset1:20
	ds_read2st64_b32 v[58:59], v52 offset0:24 offset1:28
	v_ashrrev_i32_e32 v139, 31, v138
	s_waitcnt lgkmcnt(0)
	v_add_f32_e32 v50, 0, v50
	v_add_f32_e32 v53, v50, v51
	v_add_f32_e32 v50, v53, v54
	v_add_f32_e32 v53, v50, v55
	v_add_f32_e32 v50, v53, v56
	v_add_f32_e32 v53, v50, v57
	v_add_f32_e32 v50, v53, v58
	v_add_f32_e32 v50, v50, v59
	s_nop 1
	v_max_f32_dpp v51, v50, v50 quad_perm:[1,0,3,2] row_mask:0xf bank_mask:0xf
	s_nop 1
	v_max_f32_dpp v51, v51, v51 quad_perm:[2,3,0,1] row_mask:0xf bank_mask:0xf
	s_nop 1
	v_max_f32_dpp v51, v51, v51 row_half_mirror row_mask:0xf bank_mask:0xf
	s_nop 1
	v_max_f32_dpp v51, v51, v51 row_mirror row_mask:0xf bank_mask:0xf
	v_sub_f32_e32 v50, v50, v51
	v_mul_f32_e32 v50, 0x3fb8aa3b, v50
	v_exp_f32_e32 v50, v50
	s_nop 1
	v_add_f32_dpp v51, v50, v50 quad_perm:[1,0,3,2] row_mask:0xf bank_mask:0xf
	s_nop 1
	v_add_f32_dpp v51, v51, v51 quad_perm:[2,3,0,1] row_mask:0xf bank_mask:0xf
	s_nop 1
	v_add_f32_dpp v51, v51, v51 row_half_mirror row_mask:0xf bank_mask:0xf
	s_nop 1
	v_add_f32_dpp v51, v51, v51 row_mirror row_mask:0xf bank_mask:0xf
	v_div_scale_f32 v52, s[8:9], v51, v51, v50
	v_rcp_f32_e32 v53, v52
	s_nop 0
	v_fma_f32 v54, -v52, v53, 1.0
	v_fmac_f32_e32 v53, v54, v53
	v_div_scale_f32 v54, vcc, v50, v51, v50
	v_mul_f32_e32 v55, v54, v53
	v_fma_f32 v56, -v52, v55, v54
	v_fmac_f32_e32 v55, v56, v53
	v_fma_f32 v52, -v52, v55, v54
	v_div_fmas_f32 v52, v52, v53, v55
	v_div_fixup_f32 v52, v52, v51, v50
	v_lshlrev_b64 v[50:51], 6, v[138:139]
	v_lshl_add_u64 v[50:51], v[88:89], 0, v[50:51]
	global_store_dword v[50:51], v52, off

; #define LAS __attribute__((address_space(3)))
; __device__ __forceinline__ void tk_phase(const Frame& F0, bool with_ctx) {
;     ...
;             LAS int* buf = cb + 64 + ((bit >> 1) & 3) * 24;
;             if (F.lane == 0) { buf[F.wave * 3] = n1; buf[F.wave * 3 + 1] = n2; buf[F.wave * 3 + 2] = n3; }
;             __syncthreads();
;             int t1 = 0, t2 = 0, t3 = 0;
; #pragma unroll
;             for (int w = 0; w < 8; ++w) { t1 += buf[w * 3]; t2 += buf[w * 3 + 1]; t3 += buf[w * 3 + 2]; }
;             T = t3 >= 256 ? c3 : t1 >= 256 ? c1 : t2 >= 256 ? c2 : T;
.LBB0_1283:
	s_or_b64 exec, exec, s[18:19]
	v_mov_b32_e32 v5, s29
	s_waitcnt lgkmcnt(0)
	s_barrier
	ds_read_b96 v[36:38], v5 offset:256
	ds_read_b32 v18, v5 offset:276
	ds_read_b64 v[44:45], v5 offset:280
	ds_read_b128 v[6:9], v5 offset:288
	ds_read_b96 v[40:42], v5 offset:304
	ds_read_b128 v[32:35], v5 offset:336
	ds_read2_b32 v[46:47], v5 offset0:67 offset1:68
	ds_read_b32 v48, v5 offset:324
	ds_read2_b32 v[50:51], v5 offset0:79 offset1:80
	ds_read_b64 v[52:53], v5 offset:328
	s_cmp_lt_u32 s28, 3
	s_waitcnt lgkmcnt(0)
	v_add_u32_e32 v18, v18, v38
	v_add_u32_e32 v6, v18, v6
	v_add_u32_e32 v6, v6, v9
	v_add_u32_e32 v6, v6, v42
	v_add_u32_e32 v18, v47, v37
	v_add_u32_e32 v18, v18, v45
	v_add_u32_e32 v6, v6, v48
	v_add_u32_e32 v6, v6, v32
	v_add_u32_e32 v9, v6, v35
	v_add_u32_e32 v6, v46, v36
	v_add_u32_e32 v6, v6, v44
	v_add_u32_e32 v6, v6, v7
	v_add_u32_e32 v7, v18, v8
	v_add_u32_e32 v8, v7, v41
	v_add_u32_e32 v18, v6, v40
	v_add_u32_e32 v18, v18, v50
	v_add_u32_e32 v8, v8, v51
	v_add_u32_e32 v5, v8, v53
	v_add_u32_e32 v6, v18, v52
	v_add_u32_e32 v5, v5, v34
	v_add_u32_e32 v6, v6, v33
	v_cmp_lt_i32_e32 vcc, s21, v5
	s_nop 1
	v_cndmask_b32_e32 v4, v30, v4, vcc
	v_cmp_lt_i32_e32 vcc, s21, v6
	s_nop 1
	v_cndmask_b32_e32 v2, v4, v2, vcc
	v_cmp_lt_i32_e32 vcc, s21, v9
	s_nop 1
	v_cndmask_b32_e32 v30, v2, v3, vcc
	s_cbranch_scc1 .LBB0_1290
